# k_gcn gather loop: index loads two batches ahead (second index set in free VGPRs, dest-as-address), loop-top wait removed, one vmcnt(8) per half
# baseline (speedup 1.0000x reference)
.LBB2_9:
	v_add_lshl_u32 v64, v50, s33, 2
	global_load_dword v67, v64, s[22:23] offset:16
	global_load_dword v71, v64, s[22:23] offset:20
	global_load_dword v95, v64, s[22:23] offset:24
	global_load_dword v68, v64, s[22:23] offset:28
	global_load_dword v55, v64, s[22:23] offset:4
	global_load_dword v66, v64, s[22:23] offset:8
	global_load_dword v65, v64, s[22:23] offset:12
	global_load_dword v64, v64, s[22:23]
	v_lshl_or_b32 v34, v36, 8, v54
	buffer_load_dwordx4 v[34:37], v34, s[24:27], 0 offen
	v_lshl_or_b32 v38, v38, 8, v54
	buffer_load_dwordx4 v[38:41], v38, s[24:27], 0 offen
	v_lshl_or_b32 v42, v42, 8, v54
	buffer_load_dwordx4 v[42:45], v42, s[24:27], 0 offen
	v_lshl_or_b32 v46, v46, 8, v54
	buffer_load_dwordx4 v[46:49], v46, s[24:27], 0 offen
	s_waitcnt vmcnt(4)
.Lkg_A:
	s_cmp_ge_i32 s33, s31
	s_cbranch_scc1 .Lkg_finA
	v_subrev_u32_e32 v69, s33, v53
	v_cmp_lt_i32_e64 s[34:35], 0, v69
	v_cmp_lt_i32_e64 s[36:37], 1, v69
	v_cmp_lt_i32_e64 s[38:39], 2, v69
	v_cmp_lt_i32_e64 s[40:41], 3, v69
	v_cndmask_b32_e64 v72, v70, v64, s[34:35]
	v_cndmask_b32_e64 v76, v70, v55, s[36:37]
	v_cndmask_b32_e64 v86, v70, v66, s[38:39]
	v_cndmask_b32_e64 v90, v70, v65, s[40:41]
	v_add_lshl_u32 v64, v50, s33, 2
	global_load_dword v55, v64, s[22:23] offset:36
	global_load_dword v66, v64, s[22:23] offset:40
	global_load_dword v65, v64, s[22:23] offset:44
	global_load_dword v64, v64, s[22:23] offset:32
	s_add_i32 s33, s33, 4
	v_lshl_or_b32 v72, v72, 8, v54
	buffer_load_dwordx4 v[72:75], v72, s[24:27], 0 offen
	v_lshl_or_b32 v76, v76, 8, v54
	buffer_load_dwordx4 v[76:79], v76, s[24:27], 0 offen
	v_lshl_or_b32 v86, v86, 8, v54
	buffer_load_dwordx4 v[86:89], v86, s[24:27], 0 offen
	v_lshl_or_b32 v90, v90, 8, v54
	buffer_load_dwordx4 v[90:93], v90, s[24:27], 0 offen
	s_waitcnt vmcnt(8)
	v_fma_mix_f32 v62, v34, 1.0, v62 op_sel_hi:[1,0,0]
	v_fma_mix_f32 v63, v34, 1.0, v63 op_sel:[1,0,0] op_sel_hi:[1,0,0]
	v_fma_mix_f32 v60, v35, 1.0, v60 op_sel_hi:[1,0,0]
	v_fma_mix_f32 v61, v35, 1.0, v61 op_sel:[1,0,0] op_sel_hi:[1,0,0]
	v_fma_mix_f32 v58, v36, 1.0, v58 op_sel_hi:[1,0,0]
	v_fma_mix_f32 v59, v36, 1.0, v59 op_sel:[1,0,0] op_sel_hi:[1,0,0]
	v_fma_mix_f32 v56, v37, 1.0, v56 op_sel_hi:[1,0,0]
	v_fma_mix_f32 v57, v37, 1.0, v57 op_sel:[1,0,0] op_sel_hi:[1,0,0]
	v_fma_mix_f32 v62, v38, 1.0, v62 op_sel_hi:[1,0,0]
	v_fma_mix_f32 v63, v38, 1.0, v63 op_sel:[1,0,0] op_sel_hi:[1,0,0]
	v_fma_mix_f32 v60, v39, 1.0, v60 op_sel_hi:[1,0,0]
	v_fma_mix_f32 v61, v39, 1.0, v61 op_sel:[1,0,0] op_sel_hi:[1,0,0]
	v_fma_mix_f32 v58, v40, 1.0, v58 op_sel_hi:[1,0,0]
	v_fma_mix_f32 v59, v40, 1.0, v59 op_sel:[1,0,0] op_sel_hi:[1,0,0]
	v_fma_mix_f32 v56, v41, 1.0, v56 op_sel_hi:[1,0,0]
	v_fma_mix_f32 v57, v41, 1.0, v57 op_sel:[1,0,0] op_sel_hi:[1,0,0]
	v_fma_mix_f32 v62, v42, 1.0, v62 op_sel_hi:[1,0,0]
	v_fma_mix_f32 v63, v42, 1.0, v63 op_sel:[1,0,0] op_sel_hi:[1,0,0]
	v_fma_mix_f32 v60, v43, 1.0, v60 op_sel_hi:[1,0,0]
	v_fma_mix_f32 v61, v43, 1.0, v61 op_sel:[1,0,0] op_sel_hi:[1,0,0]
	v_fma_mix_f32 v58, v44, 1.0, v58 op_sel_hi:[1,0,0]
	v_fma_mix_f32 v59, v44, 1.0, v59 op_sel:[1,0,0] op_sel_hi:[1,0,0]
	v_fma_mix_f32 v56, v45, 1.0, v56 op_sel_hi:[1,0,0]
	v_fma_mix_f32 v57, v45, 1.0, v57 op_sel:[1,0,0] op_sel_hi:[1,0,0]
	v_fma_mix_f32 v62, v46, 1.0, v62 op_sel_hi:[1,0,0]
	v_fma_mix_f32 v63, v46, 1.0, v63 op_sel:[1,0,0] op_sel_hi:[1,0,0]
	v_fma_mix_f32 v60, v47, 1.0, v60 op_sel_hi:[1,0,0]
	v_fma_mix_f32 v61, v47, 1.0, v61 op_sel:[1,0,0] op_sel_hi:[1,0,0]
	v_fma_mix_f32 v58, v48, 1.0, v58 op_sel_hi:[1,0,0]
	v_fma_mix_f32 v59, v48, 1.0, v59 op_sel:[1,0,0] op_sel_hi:[1,0,0]
	v_fma_mix_f32 v56, v49, 1.0, v56 op_sel_hi:[1,0,0]
	v_fma_mix_f32 v57, v49, 1.0, v57 op_sel:[1,0,0] op_sel_hi:[1,0,0]
.Lkg_B:
	s_cmp_ge_i32 s33, s31
	s_cbranch_scc1 .Lkg_finB
	v_subrev_u32_e32 v69, s33, v53
	v_cmp_lt_i32_e64 s[34:35], 0, v69
	v_cmp_lt_i32_e64 s[36:37], 1, v69
	v_cmp_lt_i32_e64 s[38:39], 2, v69
	v_cmp_lt_i32_e64 s[40:41], 3, v69
	v_cndmask_b32_e64 v34, v70, v67, s[34:35]
	v_cndmask_b32_e64 v38, v70, v71, s[36:37]
	v_cndmask_b32_e64 v42, v70, v95, s[38:39]
	v_cndmask_b32_e64 v46, v70, v68, s[40:41]
	v_add_lshl_u32 v67, v50, s33, 2
	global_load_dword v71, v67, s[22:23] offset:36
	global_load_dword v95, v67, s[22:23] offset:40
	global_load_dword v68, v67, s[22:23] offset:44
	global_load_dword v67, v67, s[22:23] offset:32
	s_add_i32 s33, s33, 4
	v_lshl_or_b32 v34, v34, 8, v54
	buffer_load_dwordx4 v[34:37], v34, s[24:27], 0 offen
	v_lshl_or_b32 v38, v38, 8, v54
	buffer_load_dwordx4 v[38:41], v38, s[24:27], 0 offen
	v_lshl_or_b32 v42, v42, 8, v54
	buffer_load_dwordx4 v[42:45], v42, s[24:27], 0 offen
	v_lshl_or_b32 v46, v46, 8, v54
	buffer_load_dwordx4 v[46:49], v46, s[24:27], 0 offen
	s_waitcnt vmcnt(8)
	v_fma_mix_f32 v62, v72, 1.0, v62 op_sel_hi:[1,0,0]
	v_fma_mix_f32 v63, v72, 1.0, v63 op_sel:[1,0,0] op_sel_hi:[1,0,0]
	v_fma_mix_f32 v60, v73, 1.0, v60 op_sel_hi:[1,0,0]
	v_fma_mix_f32 v61, v73, 1.0, v61 op_sel:[1,0,0] op_sel_hi:[1,0,0]
	v_fma_mix_f32 v58, v74, 1.0, v58 op_sel_hi:[1,0,0]
	v_fma_mix_f32 v59, v74, 1.0, v59 op_sel:[1,0,0] op_sel_hi:[1,0,0]
	v_fma_mix_f32 v56, v75, 1.0, v56 op_sel_hi:[1,0,0]
	v_fma_mix_f32 v57, v75, 1.0, v57 op_sel:[1,0,0] op_sel_hi:[1,0,0]
	v_fma_mix_f32 v62, v76, 1.0, v62 op_sel_hi:[1,0,0]
	v_fma_mix_f32 v63, v76, 1.0, v63 op_sel:[1,0,0] op_sel_hi:[1,0,0]
	v_fma_mix_f32 v60, v77, 1.0, v60 op_sel_hi:[1,0,0]
	v_fma_mix_f32 v61, v77, 1.0, v61 op_sel:[1,0,0] op_sel_hi:[1,0,0]
	v_fma_mix_f32 v58, v78, 1.0, v58 op_sel_hi:[1,0,0]
	v_fma_mix_f32 v59, v78, 1.0, v59 op_sel:[1,0,0] op_sel_hi:[1,0,0]
	v_fma_mix_f32 v56, v79, 1.0, v56 op_sel_hi:[1,0,0]
	v_fma_mix_f32 v57, v79, 1.0, v57 op_sel:[1,0,0] op_sel_hi:[1,0,0]
	v_fma_mix_f32 v62, v86, 1.0, v62 op_sel_hi:[1,0,0]
	v_fma_mix_f32 v63, v86, 1.0, v63 op_sel:[1,0,0] op_sel_hi:[1,0,0]
	v_fma_mix_f32 v60, v87, 1.0, v60 op_sel_hi:[1,0,0]
	v_fma_mix_f32 v61, v87, 1.0, v61 op_sel:[1,0,0] op_sel_hi:[1,0,0]
	v_fma_mix_f32 v58, v88, 1.0, v58 op_sel_hi:[1,0,0]
	v_fma_mix_f32 v59, v88, 1.0, v59 op_sel:[1,0,0] op_sel_hi:[1,0,0]
	v_fma_mix_f32 v56, v89, 1.0, v56 op_sel_hi:[1,0,0]
	v_fma_mix_f32 v57, v89, 1.0, v57 op_sel:[1,0,0] op_sel_hi:[1,0,0]
	v_fma_mix_f32 v62, v90, 1.0, v62 op_sel_hi:[1,0,0]
	v_fma_mix_f32 v63, v90, 1.0, v63 op_sel:[1,0,0] op_sel_hi:[1,0,0]
	v_fma_mix_f32 v60, v91, 1.0, v60 op_sel_hi:[1,0,0]
	v_fma_mix_f32 v61, v91, 1.0, v61 op_sel:[1,0,0] op_sel_hi:[1,0,0]
	v_fma_mix_f32 v58, v92, 1.0, v58 op_sel_hi:[1,0,0]
	v_fma_mix_f32 v59, v92, 1.0, v59 op_sel:[1,0,0] op_sel_hi:[1,0,0]
	v_fma_mix_f32 v56, v93, 1.0, v56 op_sel_hi:[1,0,0]
	v_fma_mix_f32 v57, v93, 1.0, v57 op_sel:[1,0,0] op_sel_hi:[1,0,0]
	s_branch .Lkg_A
